# stack + MoE gate/up K-loop: first-iteration waits of units after the first do not wait for the previous unit's epilogue stores
# speedup vs baseline: 1.0064x; 1.0064x over previous
.LBB0_1729:
	s_add_u32 s22, s56, 0x100
	s_addc_u32 s23, s57, 0
	v_add_u32_e32 v130, 0x10000, v166
	v_add_u32_e32 v134, 0x14000, v166
	s_cmp_eq_u32 s18, 4
	ds_read_b128 v[154:157], v130
	ds_read_b128 v[158:161], v130 offset:1024
	ds_read_b128 v[146:149], v130 offset:2048
	ds_read_b128 v[150:153], v130 offset:3072
	ds_read_b128 v[138:141], v134
	ds_read_b128 v[142:145], v134 offset:1024
	ds_read_b128 v[130:133], v134 offset:2048
	ds_read_b128 v[134:137], v134 offset:3072
	s_cselect_b64 vcc, -1, 0
	s_and_b64 s[0:1], vcc, exec
	s_cselect_b32 s58, s30, s22
	s_cselect_b32 s59, s31, s23
	s_cselect_b32 s52, s50, s16
	s_cselect_b32 s53, s51, s17
	s_add_u32 s54, s58, 0x80
	s_addc_u32 s55, s59, 0
	s_add_u32 s0, s56, 0x80
	v_cndmask_b32_e32 v200, v171, v168, vcc
	v_cndmask_b32_e32 v201, v174, v170, vcc
	v_cndmask_b32_e32 v202, v172, v169, vcc
	v_cndmask_b32_e32 v223, v175, v173, vcc
	s_addc_u32 s1, s57, 0
	ds_read_b128 v[176:179], v167
	ds_read_b128 v[180:183], v167 offset:1024
	ds_read_b128 v[184:187], v167 offset:2048
	ds_read_b128 v[188:191], v167 offset:3072
	ds_read_b128 v[192:195], v167 offset:4096
	ds_read_b128 v[196:199], v167 offset:5120
	ds_read_b128 v[224:227], v167 offset:6144
	ds_read_b128 v[228:231], v167 offset:7168
	s_mov_b32 m0, s90
	s_nop 0
	global_load_lds_dwordx4 v172, s[0:1]
	s_mov_b32 m0, s91
	s_nop 0
	global_load_lds_dwordx4 v175, s[0:1]
	s_cmp_eq_u32 s18, -2
	s_cselect_b32 s0, s93, 1
	s_cmp_lg_u32 s0, 1
	s_cbranch_scc1 .Lgu_rx1
	s_waitcnt vmcnt(8)
	s_branch .Lgu_rx1d
.Lgu_rx1:
	s_waitcnt vmcnt(16)
.Lgu_rx1d:
	s_waitcnt lgkmcnt(0)
	s_barrier
	s_setprio 1
	s_waitcnt lgkmcnt(6)
	v_mfma_f32_16x16x128_f8f6f4 v[114:117], v[154:161], v[176:183], v[114:117]
	v_mfma_f32_16x16x128_f8f6f4 v[118:121], v[146:153], v[176:183], v[118:121]
	s_waitcnt lgkmcnt(4)
	v_mfma_f32_16x16x128_f8f6f4 v[122:125], v[154:161], v[184:191], v[122:125]
	v_mfma_f32_16x16x128_f8f6f4 v[126:129], v[146:153], v[184:191], v[126:129]
	s_waitcnt lgkmcnt(2)
	v_mfma_f32_16x16x128_f8f6f4 v[82:85], v[154:161], v[192:199], v[82:85]
	v_mfma_f32_16x16x128_f8f6f4 v[86:89], v[146:153], v[192:199], v[86:89]
	s_waitcnt lgkmcnt(0)
	v_mfma_f32_16x16x128_f8f6f4 v[90:93], v[154:161], v[224:231], v[90:93]
	v_mfma_f32_16x16x128_f8f6f4 v[94:97], v[146:153], v[224:231], v[94:97]
	s_setprio 0
	s_setprio 1
	v_mfma_f32_16x16x128_f8f6f4 v[98:101], v[138:145], v[176:183], v[98:101]
	v_mfma_f32_16x16x128_f8f6f4 v[102:105], v[130:137], v[176:183], v[102:105]
	v_mfma_f32_16x16x128_f8f6f4 v[106:109], v[138:145], v[184:191], v[106:109]
	v_mfma_f32_16x16x128_f8f6f4 v[110:113], v[130:137], v[184:191], v[110:113]
	v_mfma_f32_16x16x128_f8f6f4 v[66:69], v[138:145], v[192:199], v[66:69]
	v_mfma_f32_16x16x128_f8f6f4 v[70:73], v[130:137], v[192:199], v[70:73]
	v_mfma_f32_16x16x128_f8f6f4 v[74:77], v[138:145], v[224:231], v[74:77]
	v_mfma_f32_16x16x128_f8f6f4 v[78:81], v[130:137], v[224:231], v[78:81]
	s_setprio 0
	s_barrier
	ds_read_b128 v[176:179], v167 offset:16384
	ds_read_b128 v[180:183], v167 offset:17408
	ds_read_b128 v[184:187], v167 offset:18432
	ds_read_b128 v[188:191], v167 offset:19456
	ds_read_b128 v[192:195], v167 offset:20480
	ds_read_b128 v[196:199], v167 offset:21504
	ds_read_b128 v[224:227], v167 offset:22528
	ds_read_b128 v[228:231], v167 offset:23552
	s_mov_b32 m0, s35
	s_nop 0
	global_load_lds_dwordx4 v162, s[52:53]
	s_mov_b32 m0, s37
	s_nop 0
	global_load_lds_dwordx4 v163, s[52:53]
	s_add_u32 s0, s52, 0x20000
	s_addc_u32 s1, s53, 0
	s_mov_b32 m0, s47
	s_nop 0
	global_load_lds_dwordx4 v162, s[0:1]
	s_mov_b32 m0, s75
	s_nop 0
	global_load_lds_dwordx4 v163, s[0:1]
	s_mov_b32 m0, s34
	s_nop 0
	global_load_lds_dwordx4 v200, s[58:59]
	s_mov_b32 m0, s77
	s_nop 0
	global_load_lds_dwordx4 v201, s[58:59]
	s_cmp_eq_u32 s18, -2
	s_cselect_b32 s0, s93, 1
	s_cmp_lg_u32 s0, 1
	s_cbranch_scc1 .Lgu_rx2
	s_waitcnt vmcnt(8)
	s_branch .Lgu_rx2d

.Lgu_rx2d:
	s_waitcnt lgkmcnt(0)
	s_barrier
	s_setprio 1
	s_waitcnt lgkmcnt(6)
	v_mfma_f32_16x16x128_f8f6f4 v[50:53], v[154:161], v[176:183], v[50:53]
	v_mfma_f32_16x16x128_f8f6f4 v[54:57], v[146:153], v[176:183], v[54:57]
	s_waitcnt lgkmcnt(4)
	v_mfma_f32_16x16x128_f8f6f4 v[58:61], v[154:161], v[184:191], v[58:61]
	v_mfma_f32_16x16x128_f8f6f4 v[62:65], v[146:153], v[184:191], v[62:65]
	s_waitcnt lgkmcnt(2)
	v_mfma_f32_16x16x128_f8f6f4 v[206:209], v[154:161], v[192:199], v[18:21]
	v_mfma_f32_16x16x128_f8f6f4 v[218:221], v[146:153], v[192:199], v[22:25]
	s_waitcnt lgkmcnt(0)
	v_mfma_f32_16x16x128_f8f6f4 v[232:235], v[154:161], v[224:231], v[26:29]
	v_mfma_f32_16x16x128_f8f6f4 v[236:239], v[146:153], v[224:231], v[30:33]
	s_setprio 0
	s_setprio 1
	v_mfma_f32_16x16x128_f8f6f4 v[240:243], v[138:145], v[176:183], v[34:37]
	v_mfma_f32_16x16x128_f8f6f4 v[244:247], v[130:137], v[176:183], v[38:41]
	v_mfma_f32_16x16x128_f8f6f4 v[210:213], v[138:145], v[184:191], v[42:45]
	v_mfma_f32_16x16x128_f8f6f4 v[184:187], v[130:137], v[184:191], v[46:49]
	v_mfma_f32_16x16x128_f8f6f4 v[188:191], v[138:145], v[192:199], v[2:5]
	v_mfma_f32_16x16x128_f8f6f4 v[192:195], v[130:137], v[192:199], v[6:9]
	v_mfma_f32_16x16x128_f8f6f4 v[196:199], v[138:145], v[224:231], v[10:13]
	v_mfma_f32_16x16x128_f8f6f4 v[224:227], v[130:137], v[224:231], v[14:17]
	s_setprio 0
	s_barrier
	s_nop 4
	v_add_u32_e32 v14, 0x18000, v166
	v_add_u32_e32 v18, 0x1c000, v166
	ds_read_b128 v[2:5], v14
	ds_read_b128 v[6:9], v14 offset:1024
	ds_read_b128 v[10:13], v14 offset:2048
	ds_read_b128 v[14:17], v14 offset:3072
	ds_read_b128 v[130:133], v18
	ds_read_b128 v[134:137], v18 offset:1024
	ds_read_b128 v[138:141], v18 offset:2048
	ds_read_b128 v[142:145], v18 offset:3072
	ds_read_b128 v[18:21], v167 offset:32768
	ds_read_b128 v[22:25], v167 offset:33792
	ds_read_b128 v[26:29], v167 offset:34816
	ds_read_b128 v[30:33], v167 offset:35840
	ds_read_b128 v[34:37], v167 offset:36864
	ds_read_b128 v[38:41], v167 offset:37888
	ds_read_b128 v[42:45], v167 offset:38912
	ds_read_b128 v[46:49], v167 offset:39936
	s_mov_b32 m0, s78
	s_nop 0
	global_load_lds_dwordx4 v202, s[58:59]
	s_mov_b32 m0, s79
	s_nop 0
	global_load_lds_dwordx4 v223, s[58:59]
	s_waitcnt vmcnt(8)
	s_waitcnt lgkmcnt(0)
	s_barrier
	s_setprio 1
	s_waitcnt lgkmcnt(6)
	v_mfma_f32_16x16x128_f8f6f4 v[114:117], v[2:9], v[18:25], v[114:117]
	v_mfma_f32_16x16x128_f8f6f4 v[118:121], v[10:17], v[18:25], v[118:121]
	s_waitcnt lgkmcnt(4)
	v_mfma_f32_16x16x128_f8f6f4 v[122:125], v[2:9], v[26:33], v[122:125]
	v_mfma_f32_16x16x128_f8f6f4 v[126:129], v[10:17], v[26:33], v[126:129]
	s_waitcnt lgkmcnt(2)
	v_mfma_f32_16x16x128_f8f6f4 v[82:85], v[2:9], v[34:41], v[82:85]
	v_mfma_f32_16x16x128_f8f6f4 v[86:89], v[10:17], v[34:41], v[86:89]
	s_waitcnt lgkmcnt(0)
	v_mfma_f32_16x16x128_f8f6f4 v[90:93], v[2:9], v[42:49], v[90:93]
	v_mfma_f32_16x16x128_f8f6f4 v[94:97], v[10:17], v[42:49], v[94:97]
	s_setprio 0
	s_setprio 1
	v_mfma_f32_16x16x128_f8f6f4 v[98:101], v[130:137], v[18:25], v[98:101]
	v_mfma_f32_16x16x128_f8f6f4 v[102:105], v[138:145], v[18:25], v[102:105]
	v_mfma_f32_16x16x128_f8f6f4 v[106:109], v[130:137], v[26:33], v[106:109]
	v_mfma_f32_16x16x128_f8f6f4 v[110:113], v[138:145], v[26:33], v[110:113]
	v_mfma_f32_16x16x128_f8f6f4 v[66:69], v[130:137], v[34:41], v[66:69]
	v_mfma_f32_16x16x128_f8f6f4 v[70:73], v[138:145], v[34:41], v[70:73]
	v_mfma_f32_16x16x128_f8f6f4 v[74:77], v[130:137], v[42:49], v[74:77]
	v_mfma_f32_16x16x128_f8f6f4 v[78:81], v[138:145], v[42:49], v[78:81]
	s_setprio 0
	s_barrier
	ds_read_b128 v[38:41], v167 offset:49152
	ds_read_b128 v[42:45], v167 offset:50176
	ds_read_b128 v[146:149], v167 offset:51200
	ds_read_b128 v[150:153], v167 offset:52224
	ds_read_b128 v[154:157], v167 offset:53248
	ds_read_b128 v[158:161], v167 offset:54272
	ds_read_b128 v[176:179], v167 offset:55296
	ds_read_b128 v[180:183], v167 offset:56320
	s_add_u32 s0, s52, 0x80
	s_addc_u32 s1, s53, 0
	s_mov_b32 m0, s84
	s_nop 0
	global_load_lds_dwordx4 v162, s[0:1]
	s_mov_b32 m0, s85
	s_nop 0
	global_load_lds_dwordx4 v163, s[0:1]
	s_add_u32 s0, s52, 0x20080
	s_addc_u32 s1, s53, 0
	s_mov_b32 m0, s88
	s_nop 0
	global_load_lds_dwordx4 v162, s[0:1]
	s_mov_b32 m0, s89
	s_nop 0
	global_load_lds_dwordx4 v163, s[0:1]
	s_mov_b32 m0, s86
	s_nop 0
	global_load_lds_dwordx4 v200, s[54:55]
	s_mov_b32 m0, s87
	s_nop 0
	global_load_lds_dwordx4 v201, s[54:55]
	s_waitcnt vmcnt(8)
	s_waitcnt lgkmcnt(0)
	s_barrier
	s_setprio 1
	s_waitcnt lgkmcnt(6)
	v_mfma_f32_16x16x128_f8f6f4 v[50:53], v[2:9], v[38:45], v[50:53]
	v_mfma_f32_16x16x128_f8f6f4 v[54:57], v[10:17], v[38:45], v[54:57]
	s_waitcnt lgkmcnt(4)
	v_mfma_f32_16x16x128_f8f6f4 v[58:61], v[2:9], v[146:153], v[58:61]
	v_mfma_f32_16x16x128_f8f6f4 v[62:65], v[10:17], v[146:153], v[62:65]
	s_waitcnt lgkmcnt(2)
	v_mfma_f32_16x16x128_f8f6f4 v[18:21], v[2:9], v[154:161], v[206:209]
	v_mfma_f32_16x16x128_f8f6f4 v[22:25], v[10:17], v[154:161], v[218:221]
	s_waitcnt lgkmcnt(0)
	v_mfma_f32_16x16x128_f8f6f4 v[26:29], v[2:9], v[176:183], v[232:235]
	v_mfma_f32_16x16x128_f8f6f4 v[30:33], v[10:17], v[176:183], v[236:239]
	s_setprio 0
	s_setprio 1
	v_mfma_f32_16x16x128_f8f6f4 v[34:37], v[130:137], v[38:45], v[240:243]
	v_mfma_f32_16x16x128_f8f6f4 v[38:41], v[138:145], v[38:45], v[244:247]
	v_mfma_f32_16x16x128_f8f6f4 v[42:45], v[130:137], v[146:153], v[210:213]
	v_mfma_f32_16x16x128_f8f6f4 v[46:49], v[138:145], v[146:153], v[184:187]
	v_mfma_f32_16x16x128_f8f6f4 v[2:5], v[130:137], v[154:161], v[188:191]
	v_mfma_f32_16x16x128_f8f6f4 v[6:9], v[138:145], v[154:161], v[192:195]
	v_mfma_f32_16x16x128_f8f6f4 v[10:13], v[130:137], v[176:183], v[196:199]
	v_mfma_f32_16x16x128_f8f6f4 v[14:17], v[138:145], v[176:183], v[224:227]
	s_setprio 0
	s_barrier
	s_add_i32 s18, s18, 2
	s_add_u32 s16, s16, 0x100
	s_addc_u32 s17, s17, 0
	s_cmp_gt_u32 s18, 5
	s_mov_b64 s[56:57], s[22:23]
	s_cbranch_scc0 .LBB0_1729
	s_and_b64 vcc, exec, s[12:13]
	s_cbranch_vccz .LBB0_1732
	s_barrier
